# all result stores write-through (sc1) instead of nt/plain: less dirty L2 to flush at kernel boundaries
# speedup vs baseline: 1.0251x; 1.0109x over previous
.LBB0_16:
	v_add_co_u32_e32 v18, vcc, 0x1000, v4
	global_load_dwordx4 v[6:9], v[4:5], off nt
	s_nop 0
	v_addc_co_u32_e32 v19, vcc, 0, v5, vcc
	v_add_co_u32_e32 v20, vcc, 0x2000, v4
	s_movk_i32 s3, 0x1000
	s_nop 0
	v_addc_co_u32_e32 v21, vcc, 0, v5, vcc
	v_add_co_u32_e32 v4, vcc, 0x3000, v4
	global_load_dwordx4 v[10:13], v[18:19], off nt
	global_load_dwordx4 v[14:17], v[20:21], off nt
	v_addc_co_u32_e32 v5, vcc, 0, v5, vcc
	global_load_dwordx4 v[18:21], v[4:5], off nt
	s_waitcnt lgkmcnt(0)
	v_lshl_add_u64 v[2:3], v[2:3], 1, s[4:5]
	v_add_co_u32_e32 v4, vcc, s3, v2
	s_cmp_gt_u32 s2, 11
	s_nop 0
	v_addc_co_u32_e32 v5, vcc, 0, v3, vcc
	s_waitcnt vmcnt(3)
	v_cvt_pk_f16_f32 v6, v6, v7
	v_cvt_pk_f16_f32 v7, v8, v9
	global_store_dwordx2 v[2:3], v[6:7], off sc1
	s_waitcnt vmcnt(3)
	v_cvt_pk_f16_f32 v6, v10, v11
	v_cvt_pk_f16_f32 v7, v12, v13
	global_store_dwordx2 v[2:3], v[6:7], off offset:2048 sc1
	s_waitcnt vmcnt(3)
	v_cvt_pk_f16_f32 v2, v14, v15
	v_cvt_pk_f16_f32 v3, v16, v17
	global_store_dwordx2 v[4:5], v[2:3], off sc1
	s_waitcnt vmcnt(3)
	v_cvt_pk_f16_f32 v2, v18, v19
	v_cvt_pk_f16_f32 v3, v20, v21
	global_store_dwordx2 v[4:5], v[2:3], off offset:2048 sc1
	s_cbranch_scc1 .LBB0_26
	s_load_dwordx2 s[4:5], s[0:1], 0x48
	v_lshl_or_b32 v0, s2, 8, v0
	s_movk_i32 s2, 0x3ff
	v_cmp_lt_u32_e32 vcc, s2, v0
	v_mov_b32_e32 v1, 0
	s_and_saveexec_b64 s[2:3], vcc
	s_xor_b64 s[2:3], exec, s[2:3]
	s_cbranch_execz .LBB0_23
	s_movk_i32 s6, 0x7ff
	v_cmp_lt_u32_e32 vcc, s6, v0
	s_and_saveexec_b64 s[6:7], vcc
	s_xor_b64 s[6:7], exec, s[6:7]
	s_cbranch_execz .LBB0_20
	s_load_dwordx2 s[8:9], s[0:1], 0x40
	s_waitcnt lgkmcnt(0)
	v_lshl_add_u64 v[2:3], v[0:1], 2, s[8:9]
	s_movk_i32 s8, 0xe000
	s_mov_b32 s9, -1
	v_lshl_add_u64 v[2:3], v[2:3], 0, s[8:9]

_ZN6g128w88gemm_outEPKDF16_S1_PKfPf:
	s_load_dword s12, s[0:1], 0x20
	s_and_b32 s14, s2, 7
	s_load_dwordx8 s[4:11], s[0:1], 0x0
	s_ashr_i32 s1, s2, 3
	v_lshlrev_b32_e32 v1, 4, v0
	s_waitcnt lgkmcnt(0)
	s_lshr_b32 s0, s12, 3
	s_mul_i32 s0, s0, s14
	s_add_i32 s1, s0, s1
	s_ashr_i32 s0, s1, 31
	s_lshr_b32 s0, s0, 29
	s_add_i32 s2, s1, s0
	s_lshl_b32 s0, s2, 4
	s_movk_i32 s12, 0x70
	s_and_b32 s2, s2, 0x1fffff8
	v_bitop3_b32 v1, v1, s12, v0 bitop3:0x48
	v_lshlrev_b32_e32 v2, 8, v0
	s_mov_b32 s12, 0x1f800
	s_sub_i32 s1, s1, s2
	v_readfirstlane_b32 s3, v0
	s_and_b32 s0, s0, 0xffffff80
	v_and_or_b32 v10, v2, s12, v1
	v_or_b32_e32 v2, 0x20000, v2
	s_mov_b32 s12, 0x3f800
	s_lshl_b32 s2, s1, 7
	s_lshr_b32 s13, s3, 6
	s_bfe_u32 s19, s3, 0x20006
	v_and_or_b32 v20, v2, s12, v1
	s_lshr_b32 s12, s3, 8
	s_ashr_i32 s1, s0, 31
	s_ashr_i32 s3, s2, 31
	s_lshl_b64 s[14:15], s[0:1], 11
	s_lshl_b64 s[16:17], s[2:3], 11
	s_add_u32 s16, s6, s16
	s_addc_u32 s17, s7, s17
	s_add_u32 s14, s4, s14
	s_addc_u32 s15, s5, s15
	s_lshl_b64 s[2:3], s[2:3], 2
	s_add_u32 s4, s8, s2
	s_addc_u32 s5, s9, s3
	s_lshl_b32 s1, s19, 7
	v_bfe_u32 v22, v0, 4, 2
	s_add_u32 s4, s4, s1
	s_addc_u32 s5, s5, 0
	v_lshlrev_b32_e32 v1, 4, v22
	s_lshl_b32 s13, s13, 10
	global_load_dwordx4 v[6:9], v1, s[4:5]
	global_load_dwordx4 v[2:5], v1, s[4:5] offset:64
	s_add_i32 s5, s13, 0
	s_add_i32 s4, s5, 0x4000
	s_mov_b32 m0, s5
	s_add_i32 s6, s5, 0x2000
	global_load_lds_dwordx4 v10, s[14:15]
	s_mov_b32 m0, s4
	v_mov_b32_e32 v11, 0
	global_load_lds_dwordx4 v10, s[16:17]
	s_mov_b32 m0, s6
	s_add_i32 s7, s5, 0x6000
	v_mov_b32_e32 v21, v11
	global_load_lds_dwordx4 v20, s[14:15]
	s_mov_b32 m0, s7
	v_lshl_add_u64 v[12:13], s[14:15], 0, v[10:11]
	v_lshl_add_u64 v[14:15], s[16:17], 0, v[10:11]
	v_lshl_add_u64 v[18:19], s[16:17], 0, v[20:21]
	global_load_lds_dwordx4 v20, s[16:17]
	s_add_i32 s17, s5, 0x8000
	s_mov_b64 s[8:9], 0x80
	v_lshl_add_u64 v[16:17], s[14:15], 0, v[20:21]
	s_add_i32 s15, s5, 0xc000
	v_lshl_add_u64 v[20:21], v[12:13], 0, s[8:9]
	s_mov_b32 m0, s17
	s_add_i32 s16, s5, 0xa000
	global_load_lds_dwordx4 v[20:21], off
	v_lshl_add_u64 v[20:21], v[14:15], 0, s[8:9]
	s_mov_b32 m0, s15
	s_add_i32 s18, s5, 0xe000
	global_load_lds_dwordx4 v[20:21], off
	v_lshl_add_u64 v[20:21], v[16:17], 0, s[8:9]
	s_mov_b32 m0, s16
	s_add_i32 s22, 0, 0x10000
	global_load_lds_dwordx4 v[20:21], off
	v_lshl_add_u64 v[20:21], v[18:19], 0, s[8:9]
	s_mov_b32 m0, s18
	s_add_i32 s13, s22, s13
	global_load_lds_dwordx4 v[20:21], off
	s_waitcnt vmcnt(4)
	s_mov_b64 s[20:21], 0x100
	s_waitcnt lgkmcnt(0)
	s_barrier
	s_add_i32 s8, s5, 0x14000
	v_lshl_add_u64 v[20:21], v[12:13], 0, s[20:21]
	s_mov_b32 m0, s13
	s_add_i32 s9, s13, 0x2000
	global_load_lds_dwordx4 v[20:21], off
	v_lshl_add_u64 v[20:21], v[14:15], 0, s[20:21]
	s_mov_b32 m0, s8
	s_add_i32 s14, s5, 0x16000
	global_load_lds_dwordx4 v[20:21], off
	v_lshl_add_u64 v[20:21], v[16:17], 0, s[20:21]
	s_mov_b32 m0, s9
	v_and_b32_e32 v10, 15, v0
	global_load_lds_dwordx4 v[20:21], off
	v_lshl_add_u64 v[20:21], v[18:19], 0, s[20:21]
	s_mov_b32 m0, s14
	v_bfe_u32 v24, v0, 1, 3
	global_load_lds_dwordx4 v[20:21], off
	v_lshrrev_b32_e32 v20, 4, v0
	v_lshlrev_b32_e32 v21, 7, v10
	v_bitop3_b32 v20, v20, v24, 3 bitop3:0x6c
	v_lshl_or_b32 v23, s12, 13, v21
	v_lshl_or_b32 v72, s19, 12, v21
	v_lshlrev_b32_e32 v73, 4, v20
	v_bitop3_b32 v20, v22, v24, 4 bitop3:0x36
	v_or_b32_e32 v108, v73, v23
	v_lshlrev_b32_e32 v74, 4, v20
	v_or_b32_e32 v20, v73, v72
	v_or_b32_e32 v109, v74, v23
	v_add_u32_e32 v20, 0, v20
	v_or_b32_e32 v21, v74, v72
	v_add_u32_e32 v22, 0, v108
	v_add_u32_e32 v21, 0, v21
	ds_read_b128 v[24:27], v20 offset:16384
	ds_read_b128 v[28:31], v20 offset:18432
	ds_read_b128 v[32:35], v21 offset:16384
	ds_read_b128 v[36:39], v21 offset:18432
	v_add_u32_e32 v23, 0, v109
	ds_read_b128 v[40:43], v22
	ds_read_b128 v[44:47], v22 offset:2048
	ds_read_b128 v[48:51], v23
	ds_read_b128 v[52:55], v23 offset:2048
	ds_read_b128 v[56:59], v22 offset:4096
	ds_read_b128 v[60:63], v22 offset:6144
	ds_read_b128 v[64:67], v23 offset:4096
	ds_read_b128 v[68:71], v23 offset:6144
	v_or_b32_e32 v72, 0x4000, v72
	v_or_b32_e32 v104, v73, v72
	v_or_b32_e32 v105, v74, v72
	s_setprio 1
	s_waitcnt lgkmcnt(0)
	v_mfma_f32_16x16x32_f16 v[72:75], v[24:27], v[40:43], 0
	v_mfma_f32_16x16x32_f16 v[40:43], v[28:31], v[40:43], 0
	v_mfma_f32_16x16x32_f16 v[76:79], v[24:27], v[44:47], 0
	v_mfma_f32_16x16x32_f16 v[44:47], v[28:31], v[44:47], 0
	v_mfma_f32_16x16x32_f16 v[80:83], v[24:27], v[56:59], 0
	v_mfma_f32_16x16x32_f16 v[56:59], v[28:31], v[56:59], 0
	v_mfma_f32_16x16x32_f16 v[24:27], v[24:27], v[60:63], 0
	v_mfma_f32_16x16x32_f16 v[28:31], v[28:31], v[60:63], 0
	v_mfma_f32_16x16x32_f16 v[60:63], v[32:35], v[48:51], v[72:75]
	v_mfma_f32_16x16x32_f16 v[40:43], v[36:39], v[48:51], v[40:43]
	v_mfma_f32_16x16x32_f16 v[48:51], v[32:35], v[52:55], v[76:79]
	v_mfma_f32_16x16x32_f16 v[44:47], v[36:39], v[52:55], v[44:47]
	v_mfma_f32_16x16x32_f16 v[52:55], v[32:35], v[64:67], v[80:83]
	v_mfma_f32_16x16x32_f16 v[56:59], v[36:39], v[64:67], v[56:59]
	v_mfma_f32_16x16x32_f16 v[24:27], v[32:35], v[68:71], v[24:27]
	v_mfma_f32_16x16x32_f16 v[28:31], v[36:39], v[68:71], v[28:31]
	s_setprio 0
	s_waitcnt vmcnt(4)
	s_mov_b64 s[20:21], 0x180
	s_mov_b32 m0, s5
	s_waitcnt lgkmcnt(0)
	s_barrier
	v_lshl_add_u64 v[32:33], v[12:13], 0, s[20:21]
	global_load_lds_dwordx4 v[32:33], off
	v_lshl_add_u64 v[32:33], v[14:15], 0, s[20:21]
	s_mov_b32 m0, s4
	s_nop 0
	global_load_lds_dwordx4 v[32:33], off
	v_lshl_add_u64 v[32:33], v[16:17], 0, s[20:21]
	s_mov_b32 m0, s6
	s_nop 0
	global_load_lds_dwordx4 v[32:33], off
	v_lshl_add_u64 v[32:33], v[18:19], 0, s[20:21]
	s_mov_b32 m0, s7
	s_nop 0
	global_load_lds_dwordx4 v[32:33], off
	ds_read_b128 v[32:35], v20 offset:49152
	ds_read_b128 v[36:39], v20 offset:51200
	ds_read_b128 v[64:67], v21 offset:49152
	ds_read_b128 v[68:71], v21 offset:51200
	ds_read_b128 v[72:75], v22 offset:32768
	ds_read_b128 v[76:79], v22 offset:34816
	ds_read_b128 v[80:83], v23 offset:32768
	ds_read_b128 v[84:87], v23 offset:34816
	ds_read_b128 v[88:91], v22 offset:36864
	ds_read_b128 v[92:95], v22 offset:38912
	ds_read_b128 v[96:99], v23 offset:36864
	ds_read_b128 v[100:103], v23 offset:38912
	s_setprio 1
	s_waitcnt lgkmcnt(0)
	v_mfma_f32_16x16x32_f16 v[60:63], v[32:35], v[72:75], v[60:63]
	v_mfma_f32_16x16x32_f16 v[40:43], v[36:39], v[72:75], v[40:43]
	v_mfma_f32_16x16x32_f16 v[48:51], v[32:35], v[76:79], v[48:51]
	v_mfma_f32_16x16x32_f16 v[44:47], v[36:39], v[76:79], v[44:47]
	v_mfma_f32_16x16x32_f16 v[52:55], v[32:35], v[88:91], v[52:55]
	v_mfma_f32_16x16x32_f16 v[56:59], v[36:39], v[88:91], v[56:59]
	v_mfma_f32_16x16x32_f16 v[24:27], v[32:35], v[92:95], v[24:27]
	v_mfma_f32_16x16x32_f16 v[28:31], v[36:39], v[92:95], v[28:31]
	v_mfma_f32_16x16x32_f16 v[36:39], v[64:67], v[80:83], v[60:63]
	v_mfma_f32_16x16x32_f16 v[40:43], v[68:71], v[80:83], v[40:43]
	v_mfma_f32_16x16x32_f16 v[48:51], v[64:67], v[84:87], v[48:51]
	v_mfma_f32_16x16x32_f16 v[44:47], v[68:71], v[84:87], v[44:47]
	v_mfma_f32_16x16x32_f16 v[52:55], v[64:67], v[96:99], v[52:55]
	v_mfma_f32_16x16x32_f16 v[56:59], v[68:71], v[96:99], v[56:59]
	v_mfma_f32_16x16x32_f16 v[60:63], v[64:67], v[100:103], v[24:27]
	v_mfma_f32_16x16x32_f16 v[64:67], v[68:71], v[100:103], v[28:31]
	s_setprio 0
	s_waitcnt vmcnt(4)
	s_mov_b64 s[20:21], 0x200
	s_mov_b32 m0, s17
	s_waitcnt lgkmcnt(0)
	s_barrier
	v_lshl_add_u64 v[24:25], v[12:13], 0, s[20:21]
	global_load_lds_dwordx4 v[24:25], off
	v_lshl_add_u64 v[24:25], v[14:15], 0, s[20:21]
	s_mov_b32 m0, s15
	s_add_i32 s19, 0, 0x10800
	global_load_lds_dwordx4 v[24:25], off
	v_lshl_add_u64 v[24:25], v[16:17], 0, s[20:21]
	s_mov_b32 m0, s16
	v_add_u32_e32 v26, s19, v104
	global_load_lds_dwordx4 v[24:25], off
	v_lshl_add_u64 v[24:25], v[18:19], 0, s[20:21]
	s_mov_b32 m0, s18
	v_add_u32_e32 v27, s19, v105
	global_load_lds_dwordx4 v[24:25], off
	v_add_u32_e32 v30, s19, v108
	v_add_u32_e32 v31, s19, v109
	s_add_i32 s19, 0, 0x11000
	v_add_u32_e32 v32, s19, v108
	v_add_u32_e32 v33, s19, v109
	s_add_i32 s19, 0, 0x11800
	v_add_u32_e32 v24, s22, v104
	v_add_u32_e32 v28, s22, v108
	v_add_u32_e32 v34, s19, v108
	v_add_u32_e32 v25, s22, v105
	ds_read_b128 v[68:71], v24
	ds_read_b128 v[72:75], v25
	ds_read_b128 v[76:79], v26
	ds_read_b128 v[80:83], v27
	v_add_u32_e32 v29, s22, v109
	ds_read_b128 v[84:87], v28
	ds_read_b128 v[88:91], v29
	ds_read_b128 v[92:95], v30
	ds_read_b128 v[96:99], v31
	ds_read_b128 v[100:103], v32
	ds_read_b128 v[104:107], v33
	v_add_u32_e32 v35, s19, v109
	ds_read_b128 v[108:111], v34
	ds_read_b128 v[112:115], v35
	s_setprio 1
	s_waitcnt lgkmcnt(0)
	v_mfma_f32_16x16x32_f16 v[36:39], v[68:71], v[84:87], v[36:39]
	v_mfma_f32_16x16x32_f16 v[40:43], v[76:79], v[84:87], v[40:43]
	v_mfma_f32_16x16x32_f16 v[48:51], v[68:71], v[92:95], v[48:51]
	v_mfma_f32_16x16x32_f16 v[44:47], v[76:79], v[92:95], v[44:47]
	v_mfma_f32_16x16x32_f16 v[52:55], v[68:71], v[100:103], v[52:55]
	v_mfma_f32_16x16x32_f16 v[56:59], v[76:79], v[100:103], v[56:59]
	v_mfma_f32_16x16x32_f16 v[60:63], v[68:71], v[108:111], v[60:63]
	v_mfma_f32_16x16x32_f16 v[64:67], v[76:79], v[108:111], v[64:67]
	v_mfma_f32_16x16x32_f16 v[36:39], v[72:75], v[88:91], v[36:39]
	v_mfma_f32_16x16x32_f16 v[40:43], v[80:83], v[88:91], v[40:43]
	v_mfma_f32_16x16x32_f16 v[48:51], v[72:75], v[96:99], v[48:51]
	v_mfma_f32_16x16x32_f16 v[44:47], v[80:83], v[96:99], v[44:47]
	v_mfma_f32_16x16x32_f16 v[52:55], v[72:75], v[104:107], v[52:55]
	v_mfma_f32_16x16x32_f16 v[56:59], v[80:83], v[104:107], v[56:59]
	v_mfma_f32_16x16x32_f16 v[60:63], v[72:75], v[112:115], v[60:63]
	v_mfma_f32_16x16x32_f16 v[64:67], v[80:83], v[112:115], v[64:67]
	s_setprio 0
	s_waitcnt vmcnt(4)
	s_mov_b64 s[20:21], 0x280
	s_mov_b32 m0, s13
	s_waitcnt lgkmcnt(0)
	s_barrier
	v_lshl_add_u64 v[68:69], v[12:13], 0, s[20:21]
	global_load_lds_dwordx4 v[68:69], off
	v_lshl_add_u64 v[68:69], v[14:15], 0, s[20:21]
	s_mov_b32 m0, s8
	s_nop 0
	global_load_lds_dwordx4 v[68:69], off
	v_lshl_add_u64 v[68:69], v[16:17], 0, s[20:21]
	s_mov_b32 m0, s9
	s_nop 0
	global_load_lds_dwordx4 v[68:69], off
	v_lshl_add_u64 v[68:69], v[18:19], 0, s[20:21]
	s_mov_b32 m0, s14
	s_nop 0
	global_load_lds_dwordx4 v[68:69], off
	ds_read_b128 v[68:71], v20 offset:16384
	ds_read_b128 v[72:75], v20 offset:18432
	ds_read_b128 v[76:79], v21 offset:16384
	ds_read_b128 v[80:83], v21 offset:18432
	ds_read_b128 v[84:87], v22
	ds_read_b128 v[88:91], v22 offset:2048
	ds_read_b128 v[92:95], v23
	ds_read_b128 v[96:99], v23 offset:2048
	ds_read_b128 v[100:103], v22 offset:4096
	ds_read_b128 v[104:107], v22 offset:6144
	ds_read_b128 v[108:111], v23 offset:4096
	ds_read_b128 v[112:115], v23 offset:6144
	s_setprio 1
	s_waitcnt lgkmcnt(0)
	v_mfma_f32_16x16x32_f16 v[36:39], v[68:71], v[84:87], v[36:39]
	v_mfma_f32_16x16x32_f16 v[40:43], v[72:75], v[84:87], v[40:43]
	v_mfma_f32_16x16x32_f16 v[48:51], v[68:71], v[88:91], v[48:51]
	v_mfma_f32_16x16x32_f16 v[44:47], v[72:75], v[88:91], v[44:47]
	v_mfma_f32_16x16x32_f16 v[52:55], v[68:71], v[100:103], v[52:55]
	v_mfma_f32_16x16x32_f16 v[56:59], v[72:75], v[100:103], v[56:59]
	v_mfma_f32_16x16x32_f16 v[60:63], v[68:71], v[104:107], v[60:63]
	v_mfma_f32_16x16x32_f16 v[64:67], v[72:75], v[104:107], v[64:67]
	v_mfma_f32_16x16x32_f16 v[36:39], v[76:79], v[92:95], v[36:39]
	v_mfma_f32_16x16x32_f16 v[40:43], v[80:83], v[92:95], v[40:43]
	v_mfma_f32_16x16x32_f16 v[48:51], v[76:79], v[96:99], v[48:51]
	v_mfma_f32_16x16x32_f16 v[44:47], v[80:83], v[96:99], v[44:47]
	v_mfma_f32_16x16x32_f16 v[52:55], v[76:79], v[108:111], v[52:55]
	v_mfma_f32_16x16x32_f16 v[56:59], v[80:83], v[108:111], v[56:59]
	v_mfma_f32_16x16x32_f16 v[60:63], v[76:79], v[112:115], v[60:63]
	v_mfma_f32_16x16x32_f16 v[64:67], v[80:83], v[112:115], v[64:67]
	s_setprio 0
	s_waitcnt vmcnt(4)
	s_mov_b64 s[20:21], 0x300
	s_mov_b32 m0, s5
	s_waitcnt lgkmcnt(0)
	s_barrier
	v_lshl_add_u64 v[68:69], v[12:13], 0, s[20:21]
	global_load_lds_dwordx4 v[68:69], off
	v_lshl_add_u64 v[68:69], v[14:15], 0, s[20:21]
	s_mov_b32 m0, s4
	s_nop 0
	global_load_lds_dwordx4 v[68:69], off
	v_lshl_add_u64 v[68:69], v[16:17], 0, s[20:21]
	s_mov_b32 m0, s6
	s_nop 0
	global_load_lds_dwordx4 v[68:69], off
	v_lshl_add_u64 v[68:69], v[18:19], 0, s[20:21]
	s_mov_b32 m0, s7
	s_nop 0
	global_load_lds_dwordx4 v[68:69], off
	ds_read_b128 v[68:71], v20 offset:49152
	ds_read_b128 v[72:75], v20 offset:51200
	ds_read_b128 v[76:79], v21 offset:49152
	ds_read_b128 v[80:83], v21 offset:51200
	ds_read_b128 v[84:87], v22 offset:32768
	ds_read_b128 v[88:91], v22 offset:34816
	ds_read_b128 v[92:95], v23 offset:32768
	ds_read_b128 v[96:99], v23 offset:34816
	ds_read_b128 v[100:103], v22 offset:36864
	ds_read_b128 v[104:107], v22 offset:38912
	ds_read_b128 v[108:111], v23 offset:36864
	ds_read_b128 v[112:115], v23 offset:38912
	s_setprio 1
	s_waitcnt lgkmcnt(0)
	v_mfma_f32_16x16x32_f16 v[36:39], v[68:71], v[84:87], v[36:39]
	v_mfma_f32_16x16x32_f16 v[40:43], v[72:75], v[84:87], v[40:43]
	v_mfma_f32_16x16x32_f16 v[48:51], v[68:71], v[88:91], v[48:51]
	v_mfma_f32_16x16x32_f16 v[44:47], v[72:75], v[88:91], v[44:47]
	v_mfma_f32_16x16x32_f16 v[52:55], v[68:71], v[100:103], v[52:55]
	v_mfma_f32_16x16x32_f16 v[56:59], v[72:75], v[100:103], v[56:59]
	v_mfma_f32_16x16x32_f16 v[60:63], v[68:71], v[104:107], v[60:63]
	v_mfma_f32_16x16x32_f16 v[64:67], v[72:75], v[104:107], v[64:67]
	v_mfma_f32_16x16x32_f16 v[36:39], v[76:79], v[92:95], v[36:39]
	v_mfma_f32_16x16x32_f16 v[40:43], v[80:83], v[92:95], v[40:43]
	v_mfma_f32_16x16x32_f16 v[48:51], v[76:79], v[96:99], v[48:51]
	v_mfma_f32_16x16x32_f16 v[44:47], v[80:83], v[96:99], v[44:47]
	v_mfma_f32_16x16x32_f16 v[52:55], v[76:79], v[108:111], v[52:55]
	v_mfma_f32_16x16x32_f16 v[56:59], v[80:83], v[108:111], v[56:59]
	v_mfma_f32_16x16x32_f16 v[60:63], v[76:79], v[112:115], v[60:63]
	v_mfma_f32_16x16x32_f16 v[64:67], v[80:83], v[112:115], v[64:67]
	s_setprio 0
	s_waitcnt vmcnt(4)
	s_mov_b64 s[20:21], 0x380
	s_mov_b32 m0, s17
	s_waitcnt lgkmcnt(0)
	s_barrier
	v_lshl_add_u64 v[68:69], v[12:13], 0, s[20:21]
	global_load_lds_dwordx4 v[68:69], off
	v_lshl_add_u64 v[68:69], v[14:15], 0, s[20:21]
	s_mov_b32 m0, s15
	s_nop 0
	global_load_lds_dwordx4 v[68:69], off
	v_lshl_add_u64 v[68:69], v[16:17], 0, s[20:21]
	s_mov_b32 m0, s16
	s_nop 0
	global_load_lds_dwordx4 v[68:69], off
	v_lshl_add_u64 v[68:69], v[18:19], 0, s[20:21]
	s_mov_b32 m0, s18
	s_nop 0
	global_load_lds_dwordx4 v[68:69], off
	ds_read_b128 v[68:71], v24
	ds_read_b128 v[72:75], v25
	ds_read_b128 v[76:79], v26
	ds_read_b128 v[80:83], v27
	ds_read_b128 v[84:87], v28
	ds_read_b128 v[88:91], v29
	ds_read_b128 v[92:95], v30
	ds_read_b128 v[96:99], v31
	ds_read_b128 v[100:103], v32
	ds_read_b128 v[104:107], v33
	ds_read_b128 v[108:111], v34
	ds_read_b128 v[112:115], v35
	s_setprio 1
	s_waitcnt lgkmcnt(0)
	v_mfma_f32_16x16x32_f16 v[36:39], v[68:71], v[84:87], v[36:39]
	v_mfma_f32_16x16x32_f16 v[40:43], v[76:79], v[84:87], v[40:43]
	v_mfma_f32_16x16x32_f16 v[48:51], v[68:71], v[92:95], v[48:51]
	v_mfma_f32_16x16x32_f16 v[44:47], v[76:79], v[92:95], v[44:47]
	v_mfma_f32_16x16x32_f16 v[52:55], v[68:71], v[100:103], v[52:55]
	v_mfma_f32_16x16x32_f16 v[56:59], v[76:79], v[100:103], v[56:59]
	v_mfma_f32_16x16x32_f16 v[60:63], v[68:71], v[108:111], v[60:63]
	v_mfma_f32_16x16x32_f16 v[64:67], v[76:79], v[108:111], v[64:67]
	v_mfma_f32_16x16x32_f16 v[36:39], v[72:75], v[88:91], v[36:39]
	v_mfma_f32_16x16x32_f16 v[40:43], v[80:83], v[88:91], v[40:43]
	v_mfma_f32_16x16x32_f16 v[48:51], v[72:75], v[96:99], v[48:51]
	v_mfma_f32_16x16x32_f16 v[44:47], v[80:83], v[96:99], v[44:47]
	v_mfma_f32_16x16x32_f16 v[52:55], v[72:75], v[104:107], v[52:55]
	v_mfma_f32_16x16x32_f16 v[56:59], v[80:83], v[104:107], v[56:59]
	v_mfma_f32_16x16x32_f16 v[60:63], v[72:75], v[112:115], v[60:63]
	v_mfma_f32_16x16x32_f16 v[64:67], v[80:83], v[112:115], v[64:67]
	s_setprio 0
	s_waitcnt vmcnt(4)
	s_mov_b64 s[20:21], 0x400
	s_mov_b32 m0, s13
	s_waitcnt lgkmcnt(0)
	s_barrier
	v_lshl_add_u64 v[68:69], v[12:13], 0, s[20:21]
	global_load_lds_dwordx4 v[68:69], off
	v_lshl_add_u64 v[68:69], v[14:15], 0, s[20:21]
	s_mov_b32 m0, s8
	s_nop 0
	global_load_lds_dwordx4 v[68:69], off
	v_lshl_add_u64 v[68:69], v[16:17], 0, s[20:21]
	s_mov_b32 m0, s9
	s_nop 0
	global_load_lds_dwordx4 v[68:69], off
	v_lshl_add_u64 v[68:69], v[18:19], 0, s[20:21]
	s_mov_b32 m0, s14
	s_nop 0
	global_load_lds_dwordx4 v[68:69], off
	ds_read_b128 v[68:71], v20 offset:16384
	ds_read_b128 v[72:75], v20 offset:18432
	ds_read_b128 v[76:79], v21 offset:16384
	ds_read_b128 v[80:83], v21 offset:18432
	ds_read_b128 v[84:87], v22
	ds_read_b128 v[88:91], v22 offset:2048
	ds_read_b128 v[92:95], v23
	ds_read_b128 v[96:99], v23 offset:2048
	ds_read_b128 v[100:103], v22 offset:4096
	ds_read_b128 v[104:107], v22 offset:6144
	ds_read_b128 v[108:111], v23 offset:4096
	ds_read_b128 v[112:115], v23 offset:6144
	s_setprio 1
	s_waitcnt lgkmcnt(0)
	v_mfma_f32_16x16x32_f16 v[36:39], v[68:71], v[84:87], v[36:39]
	v_mfma_f32_16x16x32_f16 v[40:43], v[72:75], v[84:87], v[40:43]
	v_mfma_f32_16x16x32_f16 v[48:51], v[68:71], v[88:91], v[48:51]
	v_mfma_f32_16x16x32_f16 v[44:47], v[72:75], v[88:91], v[44:47]
	v_mfma_f32_16x16x32_f16 v[52:55], v[68:71], v[100:103], v[52:55]
	v_mfma_f32_16x16x32_f16 v[56:59], v[72:75], v[100:103], v[56:59]
	v_mfma_f32_16x16x32_f16 v[60:63], v[68:71], v[104:107], v[60:63]
	v_mfma_f32_16x16x32_f16 v[64:67], v[72:75], v[104:107], v[64:67]
	v_mfma_f32_16x16x32_f16 v[36:39], v[76:79], v[92:95], v[36:39]
	v_mfma_f32_16x16x32_f16 v[40:43], v[80:83], v[92:95], v[40:43]
	v_mfma_f32_16x16x32_f16 v[48:51], v[76:79], v[96:99], v[48:51]
	v_mfma_f32_16x16x32_f16 v[44:47], v[80:83], v[96:99], v[44:47]
	v_mfma_f32_16x16x32_f16 v[52:55], v[76:79], v[108:111], v[52:55]
	v_mfma_f32_16x16x32_f16 v[56:59], v[80:83], v[108:111], v[56:59]
	v_mfma_f32_16x16x32_f16 v[60:63], v[76:79], v[112:115], v[60:63]
	v_mfma_f32_16x16x32_f16 v[64:67], v[80:83], v[112:115], v[64:67]
	s_setprio 0
	s_waitcnt vmcnt(4)
	s_mov_b64 s[20:21], 0x480
	s_mov_b32 m0, s5
	s_waitcnt lgkmcnt(0)
	s_barrier
	v_lshl_add_u64 v[68:69], v[12:13], 0, s[20:21]
	global_load_lds_dwordx4 v[68:69], off
	v_lshl_add_u64 v[68:69], v[14:15], 0, s[20:21]
	s_mov_b32 m0, s4
	s_nop 0
	global_load_lds_dwordx4 v[68:69], off
	v_lshl_add_u64 v[68:69], v[16:17], 0, s[20:21]
	s_mov_b32 m0, s6
	s_nop 0
	global_load_lds_dwordx4 v[68:69], off
	v_lshl_add_u64 v[68:69], v[18:19], 0, s[20:21]
	s_mov_b32 m0, s7
	s_nop 0
	global_load_lds_dwordx4 v[68:69], off
	ds_read_b128 v[68:71], v20 offset:49152
	ds_read_b128 v[72:75], v20 offset:51200
	ds_read_b128 v[76:79], v21 offset:49152
	ds_read_b128 v[80:83], v21 offset:51200
	ds_read_b128 v[84:87], v22 offset:32768
	ds_read_b128 v[88:91], v22 offset:34816
	ds_read_b128 v[92:95], v23 offset:32768
	ds_read_b128 v[96:99], v23 offset:34816
	ds_read_b128 v[100:103], v22 offset:36864
	ds_read_b128 v[104:107], v22 offset:38912
	ds_read_b128 v[108:111], v23 offset:36864
	ds_read_b128 v[112:115], v23 offset:38912
	s_setprio 1
	s_waitcnt lgkmcnt(0)
	v_mfma_f32_16x16x32_f16 v[36:39], v[68:71], v[84:87], v[36:39]
	v_mfma_f32_16x16x32_f16 v[40:43], v[72:75], v[84:87], v[40:43]
	v_mfma_f32_16x16x32_f16 v[48:51], v[68:71], v[88:91], v[48:51]
	v_mfma_f32_16x16x32_f16 v[44:47], v[72:75], v[88:91], v[44:47]
	v_mfma_f32_16x16x32_f16 v[52:55], v[68:71], v[100:103], v[52:55]
	v_mfma_f32_16x16x32_f16 v[56:59], v[72:75], v[100:103], v[56:59]
	v_mfma_f32_16x16x32_f16 v[60:63], v[68:71], v[104:107], v[60:63]
	v_mfma_f32_16x16x32_f16 v[64:67], v[72:75], v[104:107], v[64:67]
	v_mfma_f32_16x16x32_f16 v[36:39], v[76:79], v[92:95], v[36:39]
	v_mfma_f32_16x16x32_f16 v[40:43], v[80:83], v[92:95], v[40:43]
	v_mfma_f32_16x16x32_f16 v[48:51], v[76:79], v[96:99], v[48:51]
	v_mfma_f32_16x16x32_f16 v[44:47], v[80:83], v[96:99], v[44:47]
	v_mfma_f32_16x16x32_f16 v[52:55], v[76:79], v[108:111], v[52:55]
	v_mfma_f32_16x16x32_f16 v[56:59], v[80:83], v[108:111], v[56:59]
	v_mfma_f32_16x16x32_f16 v[60:63], v[76:79], v[112:115], v[60:63]
	v_mfma_f32_16x16x32_f16 v[64:67], v[80:83], v[112:115], v[64:67]
	s_setprio 0
	s_waitcnt vmcnt(4)
	s_mov_b64 s[20:21], 0x500
	s_mov_b32 m0, s17
	s_waitcnt lgkmcnt(0)
	s_barrier
	v_lshl_add_u64 v[68:69], v[12:13], 0, s[20:21]
	global_load_lds_dwordx4 v[68:69], off
	v_lshl_add_u64 v[68:69], v[14:15], 0, s[20:21]
	s_mov_b32 m0, s15
	s_nop 0
	global_load_lds_dwordx4 v[68:69], off
	v_lshl_add_u64 v[68:69], v[16:17], 0, s[20:21]
	s_mov_b32 m0, s16
	s_nop 0
	global_load_lds_dwordx4 v[68:69], off
	v_lshl_add_u64 v[68:69], v[18:19], 0, s[20:21]
	s_mov_b32 m0, s18
	s_nop 0
	global_load_lds_dwordx4 v[68:69], off
	ds_read_b128 v[68:71], v24
	ds_read_b128 v[72:75], v25
	ds_read_b128 v[76:79], v26
	ds_read_b128 v[80:83], v27
	ds_read_b128 v[84:87], v28
	ds_read_b128 v[88:91], v29
	ds_read_b128 v[92:95], v30
	ds_read_b128 v[96:99], v31
	ds_read_b128 v[100:103], v32
	ds_read_b128 v[104:107], v33
	ds_read_b128 v[108:111], v34
	ds_read_b128 v[112:115], v35
	s_setprio 1
	s_waitcnt lgkmcnt(0)
	v_mfma_f32_16x16x32_f16 v[36:39], v[68:71], v[84:87], v[36:39]
	v_mfma_f32_16x16x32_f16 v[40:43], v[76:79], v[84:87], v[40:43]
	v_mfma_f32_16x16x32_f16 v[48:51], v[68:71], v[92:95], v[48:51]
	v_mfma_f32_16x16x32_f16 v[44:47], v[76:79], v[92:95], v[44:47]
	v_mfma_f32_16x16x32_f16 v[52:55], v[68:71], v[100:103], v[52:55]
	v_mfma_f32_16x16x32_f16 v[56:59], v[76:79], v[100:103], v[56:59]
	v_mfma_f32_16x16x32_f16 v[60:63], v[68:71], v[108:111], v[60:63]
	v_mfma_f32_16x16x32_f16 v[64:67], v[76:79], v[108:111], v[64:67]
	v_mfma_f32_16x16x32_f16 v[36:39], v[72:75], v[88:91], v[36:39]
	v_mfma_f32_16x16x32_f16 v[40:43], v[80:83], v[88:91], v[40:43]
	v_mfma_f32_16x16x32_f16 v[48:51], v[72:75], v[96:99], v[48:51]
	v_mfma_f32_16x16x32_f16 v[44:47], v[80:83], v[96:99], v[44:47]
	v_mfma_f32_16x16x32_f16 v[52:55], v[72:75], v[104:107], v[52:55]
	v_mfma_f32_16x16x32_f16 v[56:59], v[80:83], v[104:107], v[56:59]
	v_mfma_f32_16x16x32_f16 v[60:63], v[72:75], v[112:115], v[60:63]
	v_mfma_f32_16x16x32_f16 v[64:67], v[80:83], v[112:115], v[64:67]
	s_setprio 0
	s_waitcnt vmcnt(4)
	s_mov_b64 s[20:21], 0x580
	s_mov_b32 m0, s13
	s_waitcnt lgkmcnt(0)
	s_barrier
	v_lshl_add_u64 v[68:69], v[12:13], 0, s[20:21]
	global_load_lds_dwordx4 v[68:69], off
	v_lshl_add_u64 v[68:69], v[14:15], 0, s[20:21]
	s_mov_b32 m0, s8
	s_nop 0
	global_load_lds_dwordx4 v[68:69], off
	v_lshl_add_u64 v[68:69], v[16:17], 0, s[20:21]
	s_mov_b32 m0, s9
	s_nop 0
	global_load_lds_dwordx4 v[68:69], off
	v_lshl_add_u64 v[68:69], v[18:19], 0, s[20:21]
	s_mov_b32 m0, s14
	s_nop 0
	global_load_lds_dwordx4 v[68:69], off
	ds_read_b128 v[68:71], v20 offset:16384
	ds_read_b128 v[72:75], v20 offset:18432
	ds_read_b128 v[76:79], v21 offset:16384
	ds_read_b128 v[80:83], v21 offset:18432
	ds_read_b128 v[84:87], v22
	ds_read_b128 v[88:91], v22 offset:2048
	ds_read_b128 v[92:95], v23
	ds_read_b128 v[96:99], v23 offset:2048
	ds_read_b128 v[100:103], v22 offset:4096
	ds_read_b128 v[104:107], v22 offset:6144
	ds_read_b128 v[108:111], v23 offset:4096
	ds_read_b128 v[112:115], v23 offset:6144
	s_setprio 1
	s_waitcnt lgkmcnt(0)
	v_mfma_f32_16x16x32_f16 v[36:39], v[68:71], v[84:87], v[36:39]
	v_mfma_f32_16x16x32_f16 v[40:43], v[72:75], v[84:87], v[40:43]
	v_mfma_f32_16x16x32_f16 v[48:51], v[68:71], v[88:91], v[48:51]
	v_mfma_f32_16x16x32_f16 v[44:47], v[72:75], v[88:91], v[44:47]
	v_mfma_f32_16x16x32_f16 v[52:55], v[68:71], v[100:103], v[52:55]
	v_mfma_f32_16x16x32_f16 v[56:59], v[72:75], v[100:103], v[56:59]
	v_mfma_f32_16x16x32_f16 v[60:63], v[68:71], v[104:107], v[60:63]
	v_mfma_f32_16x16x32_f16 v[64:67], v[72:75], v[104:107], v[64:67]
	v_mfma_f32_16x16x32_f16 v[36:39], v[76:79], v[92:95], v[36:39]
	v_mfma_f32_16x16x32_f16 v[40:43], v[80:83], v[92:95], v[40:43]
	v_mfma_f32_16x16x32_f16 v[48:51], v[76:79], v[96:99], v[48:51]
	v_mfma_f32_16x16x32_f16 v[44:47], v[80:83], v[96:99], v[44:47]
	v_mfma_f32_16x16x32_f16 v[52:55], v[76:79], v[108:111], v[52:55]
	v_mfma_f32_16x16x32_f16 v[56:59], v[80:83], v[108:111], v[56:59]
	v_mfma_f32_16x16x32_f16 v[60:63], v[76:79], v[112:115], v[60:63]
	v_mfma_f32_16x16x32_f16 v[64:67], v[80:83], v[112:115], v[64:67]
	s_setprio 0
	s_waitcnt vmcnt(4)
	s_mov_b64 s[20:21], 0x600
	s_mov_b32 m0, s5
	s_waitcnt lgkmcnt(0)
	s_barrier
	v_lshl_add_u64 v[68:69], v[12:13], 0, s[20:21]
	global_load_lds_dwordx4 v[68:69], off
	v_lshl_add_u64 v[68:69], v[14:15], 0, s[20:21]
	s_mov_b32 m0, s4
	s_nop 0
	global_load_lds_dwordx4 v[68:69], off
	v_lshl_add_u64 v[68:69], v[16:17], 0, s[20:21]
	s_mov_b32 m0, s6
	s_nop 0
	global_load_lds_dwordx4 v[68:69], off
	v_lshl_add_u64 v[68:69], v[18:19], 0, s[20:21]
	s_mov_b32 m0, s7
	s_nop 0
	global_load_lds_dwordx4 v[68:69], off
	ds_read_b128 v[68:71], v20 offset:49152
	ds_read_b128 v[72:75], v20 offset:51200
	ds_read_b128 v[76:79], v21 offset:49152
	ds_read_b128 v[80:83], v21 offset:51200
	ds_read_b128 v[84:87], v22 offset:32768
	ds_read_b128 v[88:91], v22 offset:34816
	ds_read_b128 v[92:95], v23 offset:32768
	ds_read_b128 v[96:99], v23 offset:34816
	ds_read_b128 v[100:103], v22 offset:36864
	ds_read_b128 v[104:107], v22 offset:38912
	ds_read_b128 v[108:111], v23 offset:36864
	ds_read_b128 v[112:115], v23 offset:38912
	s_setprio 1
	s_waitcnt lgkmcnt(0)
	v_mfma_f32_16x16x32_f16 v[36:39], v[68:71], v[84:87], v[36:39]
	v_mfma_f32_16x16x32_f16 v[40:43], v[72:75], v[84:87], v[40:43]
	v_mfma_f32_16x16x32_f16 v[48:51], v[68:71], v[88:91], v[48:51]
	v_mfma_f32_16x16x32_f16 v[44:47], v[72:75], v[88:91], v[44:47]
	v_mfma_f32_16x16x32_f16 v[52:55], v[68:71], v[100:103], v[52:55]
	v_mfma_f32_16x16x32_f16 v[56:59], v[72:75], v[100:103], v[56:59]
	v_mfma_f32_16x16x32_f16 v[60:63], v[68:71], v[104:107], v[60:63]
	v_mfma_f32_16x16x32_f16 v[64:67], v[72:75], v[104:107], v[64:67]
	v_mfma_f32_16x16x32_f16 v[36:39], v[76:79], v[92:95], v[36:39]
	v_mfma_f32_16x16x32_f16 v[40:43], v[80:83], v[92:95], v[40:43]
	v_mfma_f32_16x16x32_f16 v[48:51], v[76:79], v[96:99], v[48:51]
	v_mfma_f32_16x16x32_f16 v[44:47], v[80:83], v[96:99], v[44:47]
	v_mfma_f32_16x16x32_f16 v[52:55], v[76:79], v[108:111], v[52:55]
	v_mfma_f32_16x16x32_f16 v[56:59], v[80:83], v[108:111], v[56:59]
	v_mfma_f32_16x16x32_f16 v[60:63], v[76:79], v[112:115], v[60:63]
	v_mfma_f32_16x16x32_f16 v[64:67], v[80:83], v[112:115], v[64:67]
	s_setprio 0
	s_waitcnt vmcnt(4)
	s_mov_b64 s[20:21], 0x680
	s_mov_b32 m0, s17
	s_waitcnt lgkmcnt(0)
	s_barrier
	v_lshl_add_u64 v[68:69], v[12:13], 0, s[20:21]
	global_load_lds_dwordx4 v[68:69], off
	v_lshl_add_u64 v[68:69], v[14:15], 0, s[20:21]
	s_mov_b32 m0, s15
	s_nop 0
	global_load_lds_dwordx4 v[68:69], off
	v_lshl_add_u64 v[68:69], v[16:17], 0, s[20:21]
	s_mov_b32 m0, s16
	s_nop 0
	global_load_lds_dwordx4 v[68:69], off
	v_lshl_add_u64 v[68:69], v[18:19], 0, s[20:21]
	s_mov_b32 m0, s18
	s_nop 0
	global_load_lds_dwordx4 v[68:69], off
	ds_read_b128 v[68:71], v24
	ds_read_b128 v[72:75], v25
	ds_read_b128 v[76:79], v26
	ds_read_b128 v[80:83], v27
	ds_read_b128 v[84:87], v28
	ds_read_b128 v[88:91], v29
	ds_read_b128 v[92:95], v30
	ds_read_b128 v[96:99], v31
	ds_read_b128 v[100:103], v32
	ds_read_b128 v[104:107], v33
	ds_read_b128 v[108:111], v34
	ds_read_b128 v[112:115], v35
	s_setprio 1
	s_waitcnt lgkmcnt(0)
	v_mfma_f32_16x16x32_f16 v[36:39], v[68:71], v[84:87], v[36:39]
	v_mfma_f32_16x16x32_f16 v[40:43], v[76:79], v[84:87], v[40:43]
	v_mfma_f32_16x16x32_f16 v[48:51], v[68:71], v[92:95], v[48:51]
	v_mfma_f32_16x16x32_f16 v[44:47], v[76:79], v[92:95], v[44:47]
	v_mfma_f32_16x16x32_f16 v[52:55], v[68:71], v[100:103], v[52:55]
	v_mfma_f32_16x16x32_f16 v[56:59], v[76:79], v[100:103], v[56:59]
	v_mfma_f32_16x16x32_f16 v[60:63], v[68:71], v[108:111], v[60:63]
	v_mfma_f32_16x16x32_f16 v[64:67], v[76:79], v[108:111], v[64:67]
	v_mfma_f32_16x16x32_f16 v[36:39], v[72:75], v[88:91], v[36:39]
	v_mfma_f32_16x16x32_f16 v[40:43], v[80:83], v[88:91], v[40:43]
	v_mfma_f32_16x16x32_f16 v[48:51], v[72:75], v[96:99], v[48:51]
	v_mfma_f32_16x16x32_f16 v[44:47], v[80:83], v[96:99], v[44:47]
	v_mfma_f32_16x16x32_f16 v[52:55], v[72:75], v[104:107], v[52:55]
	v_mfma_f32_16x16x32_f16 v[56:59], v[80:83], v[104:107], v[56:59]
	v_mfma_f32_16x16x32_f16 v[60:63], v[72:75], v[112:115], v[60:63]
	v_mfma_f32_16x16x32_f16 v[64:67], v[80:83], v[112:115], v[64:67]
	s_setprio 0
	s_waitcnt vmcnt(4)
	s_mov_b64 s[16:17], 0x700
	s_mov_b32 m0, s13
	s_waitcnt lgkmcnt(0)
	s_barrier
	v_lshl_add_u64 v[68:69], v[12:13], 0, s[16:17]
	global_load_lds_dwordx4 v[68:69], off
	v_lshl_add_u64 v[68:69], v[14:15], 0, s[16:17]
	s_mov_b32 m0, s8
	s_nop 0
	global_load_lds_dwordx4 v[68:69], off
	v_lshl_add_u64 v[68:69], v[16:17], 0, s[16:17]
	s_mov_b32 m0, s9
	s_nop 0
	global_load_lds_dwordx4 v[68:69], off
	v_lshl_add_u64 v[68:69], v[18:19], 0, s[16:17]
	s_mov_b32 m0, s14
	s_nop 0
	global_load_lds_dwordx4 v[68:69], off
	ds_read_b128 v[68:71], v20 offset:16384
	ds_read_b128 v[72:75], v20 offset:18432
	ds_read_b128 v[76:79], v21 offset:16384
	ds_read_b128 v[80:83], v21 offset:18432
	ds_read_b128 v[84:87], v22
	ds_read_b128 v[88:91], v22 offset:2048
	ds_read_b128 v[92:95], v23
	ds_read_b128 v[96:99], v23 offset:2048
	ds_read_b128 v[100:103], v22 offset:4096
	ds_read_b128 v[104:107], v22 offset:6144
	ds_read_b128 v[108:111], v23 offset:4096
	ds_read_b128 v[112:115], v23 offset:6144
	s_setprio 1
	s_waitcnt lgkmcnt(0)
	v_mfma_f32_16x16x32_f16 v[36:39], v[68:71], v[84:87], v[36:39]
	v_mfma_f32_16x16x32_f16 v[40:43], v[72:75], v[84:87], v[40:43]
	v_mfma_f32_16x16x32_f16 v[48:51], v[68:71], v[88:91], v[48:51]
	v_mfma_f32_16x16x32_f16 v[44:47], v[72:75], v[88:91], v[44:47]
	v_mfma_f32_16x16x32_f16 v[52:55], v[68:71], v[100:103], v[52:55]
	v_mfma_f32_16x16x32_f16 v[56:59], v[72:75], v[100:103], v[56:59]
	v_mfma_f32_16x16x32_f16 v[60:63], v[68:71], v[104:107], v[60:63]
	v_mfma_f32_16x16x32_f16 v[64:67], v[72:75], v[104:107], v[64:67]
	v_mfma_f32_16x16x32_f16 v[36:39], v[76:79], v[92:95], v[36:39]
	v_mfma_f32_16x16x32_f16 v[40:43], v[80:83], v[92:95], v[40:43]
	v_mfma_f32_16x16x32_f16 v[48:51], v[76:79], v[96:99], v[48:51]
	v_mfma_f32_16x16x32_f16 v[44:47], v[80:83], v[96:99], v[44:47]
	v_mfma_f32_16x16x32_f16 v[52:55], v[76:79], v[108:111], v[52:55]
	v_mfma_f32_16x16x32_f16 v[56:59], v[80:83], v[108:111], v[56:59]
	v_mfma_f32_16x16x32_f16 v[60:63], v[76:79], v[112:115], v[60:63]
	v_mfma_f32_16x16x32_f16 v[64:67], v[80:83], v[112:115], v[64:67]
	s_setprio 0
	s_waitcnt vmcnt(4)
	s_mov_b64 s[8:9], 0x780
	s_mov_b32 m0, s5
	s_waitcnt lgkmcnt(0)
	s_barrier
	v_lshl_add_u64 v[12:13], v[12:13], 0, s[8:9]
	global_load_lds_dwordx4 v[12:13], off
	v_lshl_add_u64 v[12:13], v[14:15], 0, s[8:9]
	s_mov_b32 m0, s4
	s_nop 0
	global_load_lds_dwordx4 v[12:13], off
	v_lshl_add_u64 v[12:13], v[16:17], 0, s[8:9]
	s_mov_b32 m0, s6
	s_nop 0
	global_load_lds_dwordx4 v[12:13], off
	v_lshl_add_u64 v[12:13], v[18:19], 0, s[8:9]
	s_mov_b32 m0, s7
	s_nop 0
	global_load_lds_dwordx4 v[12:13], off
	ds_read_b128 v[12:15], v20 offset:49152
	ds_read_b128 v[16:19], v20 offset:51200
	ds_read_b128 v[68:71], v21 offset:49152
	ds_read_b128 v[72:75], v21 offset:51200
	ds_read_b128 v[76:79], v22 offset:32768
	ds_read_b128 v[80:83], v22 offset:34816
	ds_read_b128 v[84:87], v23 offset:32768
	ds_read_b128 v[88:91], v23 offset:34816
	ds_read_b128 v[92:95], v22 offset:36864
	ds_read_b128 v[96:99], v22 offset:38912
	ds_read_b128 v[100:103], v23 offset:36864
	ds_read_b128 v[104:107], v23 offset:38912
	s_setprio 1
	s_waitcnt lgkmcnt(0)
	v_mfma_f32_16x16x32_f16 v[36:39], v[12:15], v[76:79], v[36:39]
	v_mfma_f32_16x16x32_f16 v[40:43], v[16:19], v[76:79], v[40:43]
	v_mfma_f32_16x16x32_f16 v[48:51], v[12:15], v[80:83], v[48:51]
	v_mfma_f32_16x16x32_f16 v[44:47], v[16:19], v[80:83], v[44:47]
	v_mfma_f32_16x16x32_f16 v[52:55], v[12:15], v[92:95], v[52:55]
	v_mfma_f32_16x16x32_f16 v[56:59], v[16:19], v[92:95], v[56:59]
	v_mfma_f32_16x16x32_f16 v[12:15], v[12:15], v[96:99], v[60:63]
	v_mfma_f32_16x16x32_f16 v[16:19], v[16:19], v[96:99], v[64:67]
	v_mfma_f32_16x16x32_f16 v[36:39], v[68:71], v[84:87], v[36:39]
	v_mfma_f32_16x16x32_f16 v[40:43], v[72:75], v[84:87], v[40:43]
	v_mfma_f32_16x16x32_f16 v[48:51], v[68:71], v[88:91], v[48:51]
	v_mfma_f32_16x16x32_f16 v[44:47], v[72:75], v[88:91], v[44:47]
	v_mfma_f32_16x16x32_f16 v[52:55], v[68:71], v[100:103], v[52:55]
	v_mfma_f32_16x16x32_f16 v[56:59], v[72:75], v[100:103], v[56:59]
	v_mfma_f32_16x16x32_f16 v[12:15], v[68:71], v[104:107], v[12:15]
	v_mfma_f32_16x16x32_f16 v[16:19], v[72:75], v[104:107], v[16:19]
	s_setprio 0
	s_waitcnt vmcnt(4)
	s_waitcnt lgkmcnt(0)
	s_barrier
	ds_read_b128 v[60:63], v35
	ds_read_b128 v[64:67], v34
	ds_read_b128 v[68:71], v33
	ds_read_b128 v[32:35], v32
	ds_read_b128 v[72:75], v31
	ds_read_b128 v[76:79], v30
	ds_read_b128 v[80:83], v29
	ds_read_b128 v[28:31], v28
	ds_read_b128 v[84:87], v27
	ds_read_b128 v[88:91], v26
	ds_read_b128 v[92:95], v25
	ds_read_b128 v[24:27], v24
	s_setprio 1
	s_waitcnt lgkmcnt(0)
	v_mfma_f32_16x16x32_f16 v[36:39], v[24:27], v[28:31], v[36:39]
	v_mfma_f32_16x16x32_f16 v[28:31], v[88:91], v[28:31], v[40:43]
	v_mfma_f32_16x16x32_f16 v[40:43], v[24:27], v[76:79], v[48:51]
	v_mfma_f32_16x16x32_f16 v[44:47], v[88:91], v[76:79], v[44:47]
	v_mfma_f32_16x16x32_f16 v[48:51], v[24:27], v[32:35], v[52:55]
	v_mfma_f32_16x16x32_f16 v[32:35], v[88:91], v[32:35], v[56:59]
	v_mfma_f32_16x16x32_f16 v[12:15], v[24:27], v[64:67], v[12:15]
	v_mfma_f32_16x16x32_f16 v[16:19], v[88:91], v[64:67], v[16:19]
	v_mfma_f32_16x16x32_f16 v[24:27], v[92:95], v[80:83], v[36:39]
	v_mfma_f32_16x16x32_f16 v[28:31], v[84:87], v[80:83], v[28:31]
	v_mfma_f32_16x16x32_f16 v[36:39], v[92:95], v[72:75], v[40:43]
	v_mfma_f32_16x16x32_f16 v[40:43], v[84:87], v[72:75], v[44:47]
	v_mfma_f32_16x16x32_f16 v[44:47], v[92:95], v[68:71], v[48:51]
	v_mfma_f32_16x16x32_f16 v[32:35], v[84:87], v[68:71], v[32:35]
	v_mfma_f32_16x16x32_f16 v[12:15], v[92:95], v[60:63], v[12:15]
	v_mfma_f32_16x16x32_f16 v[16:19], v[84:87], v[60:63], v[16:19]
	s_setprio 0
	s_waitcnt vmcnt(0)
	s_waitcnt lgkmcnt(0)
	s_barrier
	ds_read_b128 v[48:51], v23 offset:6144
	ds_read_b128 v[52:55], v23 offset:4096
	ds_read_b128 v[56:59], v22 offset:6144
	ds_read_b128 v[60:63], v22 offset:4096
	ds_read_b128 v[64:67], v23 offset:2048
	ds_read_b128 v[68:71], v23
	ds_read_b128 v[72:75], v22 offset:2048
	ds_read_b128 v[76:79], v22
	ds_read_b128 v[80:83], v21 offset:18432
	ds_read_b128 v[84:87], v21 offset:16384
	ds_read_b128 v[88:91], v20 offset:18432
	ds_read_b128 v[20:23], v20 offset:16384
	s_setprio 1
	s_waitcnt lgkmcnt(0)
	v_mfma_f32_16x16x32_f16 v[24:27], v[20:23], v[76:79], v[24:27]
	v_mfma_f32_16x16x32_f16 v[28:31], v[88:91], v[76:79], v[28:31]
	v_mfma_f32_16x16x32_f16 v[36:39], v[20:23], v[72:75], v[36:39]
	v_mfma_f32_16x16x32_f16 v[40:43], v[88:91], v[72:75], v[40:43]
	v_mfma_f32_16x16x32_f16 v[44:47], v[20:23], v[60:63], v[44:47]
	v_mfma_f32_16x16x32_f16 v[32:35], v[88:91], v[60:63], v[32:35]
	v_mfma_f32_16x16x32_f16 v[12:15], v[20:23], v[56:59], v[12:15]
	v_mfma_f32_16x16x32_f16 v[16:19], v[88:91], v[56:59], v[16:19]
	v_mfma_f32_16x16x32_f16 v[20:23], v[84:87], v[68:71], v[24:27]
	v_mfma_f32_16x16x32_f16 v[24:27], v[80:83], v[68:71], v[28:31]
	v_mfma_f32_16x16x32_f16 v[28:31], v[84:87], v[64:67], v[36:39]
	v_mfma_f32_16x16x32_f16 v[36:39], v[80:83], v[64:67], v[40:43]
	v_mfma_f32_16x16x32_f16 v[40:43], v[84:87], v[52:55], v[44:47]
	v_mfma_f32_16x16x32_f16 v[32:35], v[80:83], v[52:55], v[32:35]
	v_mfma_f32_16x16x32_f16 v[12:15], v[84:87], v[48:51], v[12:15]
	v_mfma_f32_16x16x32_f16 v[16:19], v[80:83], v[48:51], v[16:19]
	s_setprio 0
	v_lshl_or_b32 v10, s12, 6, v10
	s_movk_i32 s4, 0x210
	s_add_i32 s1, s1, 0
	v_mul_lo_u32 v10, v10, s4
	s_waitcnt vmcnt(0)
	v_pk_add_f32 v[22:23], v[8:9], v[22:23]
	v_pk_add_f32 v[20:21], v[6:7], v[20:21]
	v_add3_u32 v1, s1, v1, v10
	s_waitcnt lgkmcnt(0)
	s_barrier
	ds_write_b128 v1, v[20:23]
	v_pk_add_f32 v[22:23], v[8:9], v[30:31]
	v_pk_add_f32 v[20:21], v[6:7], v[28:29]
	ds_write_b128 v1, v[20:23] offset:8448
	v_pk_add_f32 v[22:23], v[8:9], v[42:43]
	v_pk_add_f32 v[20:21], v[6:7], v[40:41]
	v_pk_add_f32 v[8:9], v[8:9], v[14:15]
	v_pk_add_f32 v[6:7], v[6:7], v[12:13]
	ds_write_b128 v1, v[6:9] offset:25344
	v_pk_add_f32 v[8:9], v[4:5], v[26:27]
	v_pk_add_f32 v[6:7], v[2:3], v[24:25]
	ds_write_b128 v1, v[6:9] offset:64
	v_pk_add_f32 v[8:9], v[4:5], v[38:39]
	v_pk_add_f32 v[6:7], v[2:3], v[36:37]
	ds_write_b128 v1, v[6:9] offset:8512
	v_pk_add_f32 v[8:9], v[4:5], v[34:35]
	v_pk_add_f32 v[6:7], v[2:3], v[32:33]
	v_pk_add_f32 v[4:5], v[4:5], v[18:19]
	v_pk_add_f32 v[2:3], v[2:3], v[16:17]
	ds_write_b128 v1, v[20:23] offset:16896
	ds_write_b128 v1, v[6:9] offset:16960
	ds_write_b128 v1, v[2:5] offset:25408
	v_and_b32_e32 v1, 31, v0
	v_lshlrev_b32_e32 v10, 4, v1
	v_add_u32_e32 v1, 0, v10
	v_lshrrev_b32_e32 v6, 5, v0
	s_waitcnt lgkmcnt(0)
	s_barrier
	v_mad_u32_u24 v20, v6, s4, v1
	ds_read_b128 v[2:5], v20
	s_add_u32 s2, s10, s2
	v_or_b32_e32 v16, s0, v6
	s_addc_u32 s3, s11, s3
	v_ashrrev_i32_e32 v17, 31, v16
	v_lshl_add_u64 v[14:15], s[2:3], 0, v[10:11]
	v_lshlrev_b64 v[6:7], 12, v[16:17]
	v_lshl_add_u64 v[10:11], v[14:15], 0, v[6:7]
	ds_read_b128 v[6:9], v20 offset:16896
	s_waitcnt lgkmcnt(1)
	global_store_dwordx4 v[10:11], v[2:5], off sc1
	s_nop 1
	v_or_b32_e32 v2, 0x200, v0
	v_lshrrev_b32_e32 v10, 5, v2
	v_mad_u32_u24 v2, v10, s4, v1
	v_or_b32_e32 v10, s0, v10
	ds_read_b128 v[2:5], v2
	v_ashrrev_i32_e32 v11, 31, v10
	v_lshlrev_b64 v[10:11], 12, v[10:11]
	v_lshl_add_u64 v[18:19], v[14:15], 0, v[10:11]
	v_or_b32_e32 v10, 0x600, v0
	v_lshrrev_b32_e32 v17, 5, v10
	v_mad_u32_u24 v10, v17, s4, v1
	ds_read_b128 v[10:13], v10
	s_waitcnt lgkmcnt(1)
	global_store_dwordx4 v[18:19], v[2:5], off sc1
	s_nop 1
	v_or_b32_e32 v2, 32, v16
	v_ashrrev_i32_e32 v3, 31, v2
	v_lshlrev_b64 v[2:3], 12, v[2:3]
	v_lshl_add_u64 v[2:3], v[14:15], 0, v[2:3]
	global_store_dwordx4 v[2:3], v[6:9], off sc1
	v_or_b32_e32 v2, s0, v17
	v_ashrrev_i32_e32 v3, 31, v2
	v_lshlrev_b64 v[2:3], 12, v[2:3]
	v_lshl_add_u64 v[2:3], v[14:15], 0, v[2:3]
	s_waitcnt lgkmcnt(0)
	global_store_dwordx4 v[2:3], v[10:13], off sc1
	ds_read_b128 v[2:5], v20 offset:33792
	v_or_b32_e32 v6, 64, v16
	v_ashrrev_i32_e32 v7, 31, v6
	v_lshlrev_b64 v[6:7], 12, v[6:7]
	v_lshl_add_u64 v[10:11], v[14:15], 0, v[6:7]
	ds_read_b128 v[6:9], v20 offset:50688
	s_waitcnt lgkmcnt(1)
	global_store_dwordx4 v[10:11], v[2:5], off sc1
	s_nop 1
	v_or_b32_e32 v2, 0xa00, v0
	v_lshrrev_b32_e32 v10, 5, v2
	v_mad_u32_u24 v2, v10, s4, v1
	v_or_b32_e32 v10, s0, v10
	v_or_b32_e32 v0, 0xe00, v0
	v_ashrrev_i32_e32 v11, 31, v10
	v_lshrrev_b32_e32 v17, 5, v0
	ds_read_b128 v[2:5], v2
	v_lshlrev_b64 v[10:11], 12, v[10:11]
	v_mad_u32_u24 v0, v17, s4, v1
	v_lshl_add_u64 v[18:19], v[14:15], 0, v[10:11]
	ds_read_b128 v[10:13], v0
	v_or_b32_e32 v0, 0x60, v16
	v_ashrrev_i32_e32 v1, 31, v0
	v_lshlrev_b64 v[0:1], 12, v[0:1]
	v_lshl_add_u64 v[0:1], v[14:15], 0, v[0:1]
	s_waitcnt lgkmcnt(1)
	global_store_dwordx4 v[18:19], v[2:5], off sc1
	global_store_dwordx4 v[0:1], v[6:9], off sc1
	v_or_b32_e32 v0, s0, v17
	v_ashrrev_i32_e32 v1, 31, v0
	v_lshlrev_b64 v[0:1], 12, v[0:1]
	v_lshl_add_u64 v[0:1], v[14:15], 0, v[0:1]
	s_waitcnt lgkmcnt(0)
	global_store_dwordx4 v[0:1], v[10:13], off sc1
	s_endpgm

.LBB2_14:
	v_mul_i32_i24_e32 v3, 0x320, v3
	v_lshlrev_b32_e32 v5, 4, v5
	v_add3_u32 v3, 0, v3, v5
	ds_read_b128 v[20:23], v3
	v_cndmask_b32_e64 v3, 0, 1, s[0:1]
	v_cmp_ne_u32_e64 s[2:3], 1, v3
	v_cndmask_b32_e64 v3, 0, 1, s[4:5]
	v_lshl_add_u64 v[6:7], v[6:7], 1, s[10:11]
	v_or_b32_e32 v15, 0x200, v0
	s_andn2_b64 vcc, exec, s[0:1]
	v_cmp_ne_u32_e64 s[0:1], 1, v3
	s_waitcnt lgkmcnt(0)
	global_store_dwordx4 v[6:7], v[20:23], off sc1
	s_cbranch_vccnz .LBB2_17
	s_and_b64 vcc, exec, s[0:1]
	s_cbranch_vccnz .LBB2_18
	v_mov_b32_e32 v5, 0
	v_lshrrev_b32_e32 v3, 9, v15
	v_lshlrev_b64 v[6:7], 12, v[4:5]
	v_lshl_or_b32 v16, v3, 2, v13
	v_lshl_or_b32 v3, v3, 11, v6
	v_or_b32_e32 v6, v3, v1
	s_mov_b64 s[4:5], 0x800000
	v_lshl_add_u64 v[6:7], v[6:7], 0, s[4:5]
	v_mov_b32_e32 v3, v10
	s_cbranch_execz .LBB2_19
	s_branch .LBB2_20

.LBB2_22:
	v_lshlrev_b32_e32 v3, 1, v3
	v_mul_u32_u24_e32 v3, 0x190, v3
	v_lshlrev_b32_e32 v5, 4, v16
	v_add3_u32 v3, 0, v3, v5
	ds_read_b128 v[20:23], v3
	v_lshl_add_u64 v[6:7], v[6:7], 1, s[10:11]
	s_and_b64 vcc, exec, s[2:3]
	s_waitcnt lgkmcnt(0)
	global_store_dwordx4 v[6:7], v[20:23], off sc1
	s_cbranch_vccnz .LBB2_25
	s_and_b64 vcc, exec, s[0:1]
	s_cbranch_vccnz .LBB2_26
	v_add_u32_e32 v6, 0x200, v4
	v_mov_b32_e32 v7, 0
	v_lshlrev_b64 v[6:7], 12, v[6:7]
	v_or_b32_e32 v6, v6, v1
	s_mov_b64 s[4:5], 0x800000
	v_lshl_add_u64 v[6:7], v[6:7], 0, s[4:5]
	v_mov_b32_e32 v3, v13
	v_mov_b32_e32 v5, v10
	s_cbranch_execz .LBB2_27
	s_branch .LBB2_28

.LBB2_30:
	v_mul_i32_i24_e32 v5, 0x320, v5
	v_lshlrev_b32_e32 v3, 4, v3
	v_add3_u32 v3, 0, v5, v3
	ds_read_b128 v[20:23], v3 offset:400
	v_lshl_add_u64 v[6:7], v[6:7], 1, s[10:11]
	s_and_b64 vcc, exec, s[2:3]
	v_or_b32_e32 v16, 0x600, v0
	s_waitcnt lgkmcnt(0)
	global_store_dwordx4 v[6:7], v[20:23], off sc1
	s_cbranch_vccnz .LBB2_33
	s_and_b64 vcc, exec, s[0:1]
	s_cbranch_vccnz .LBB2_34
	v_lshl_add_u32 v4, 1, 9, v4
	v_mov_b32_e32 v5, 0
	v_bfe_u32 v6, v16, 9, 1
	v_lshlrev_b64 v[4:5], 12, v[4:5]
	v_lshl_or_b32 v4, v6, 11, v4
	v_or_b32_e32 v4, v4, v1
	s_mov_b64 s[0:1], 0x800000
	v_lshl_or_b32 v3, v6, 2, v13
	v_lshl_add_u64 v[4:5], v[4:5], 0, s[0:1]
	v_mov_b32_e32 v6, v10
	s_cbranch_execz .LBB2_35
	s_branch .LBB2_36

.LBB2_38:
	v_lshl_or_b32 v2, v6, 1, 1
	v_mul_u32_u24_e32 v2, 0x190, v2
	v_lshlrev_b32_e32 v3, 4, v3
	v_add3_u32 v2, 0, v2, v3
	ds_read_b128 v[22:25], v2
	s_add_i32 s2, s7, 1
	s_cmp_gt_u32 s24, 4
	s_cselect_b64 s[4:5], -1, 0
	s_and_b32 s0, s2, 0x70
	s_cmp_lg_u32 s0, 16
	v_lshl_add_u64 v[2:3], v[4:5], 1, s[10:11]
	s_cselect_b64 s[0:1], -1, 0
	s_lshl_b32 s3, s2, 5
	s_waitcnt lgkmcnt(0)
	global_store_dwordx4 v[2:3], v[22:25], off sc1
	s_and_b32 s3, s3, 0x1e0
	s_lshl_b32 s8, s2, 11
	v_cndmask_b32_e64 v3, 0, 1, s[0:1]
	s_cmp_lt_u32 s24, 5
	v_add_u32_e32 v4, s3, v17
	v_add_u32_e32 v2, s3, v18
	v_cmp_ne_u32_e64 s[2:3], 1, v3
	s_cbranch_scc1 .LBB2_41
	s_and_b64 vcc, exec, s[2:3]
	s_cbranch_vccnz .LBB2_42
	v_mov_b32_e32 v5, 0
	v_lshlrev_b64 v[6:7], 12, v[4:5]
	v_or_b32_e32 v6, v6, v1
	s_mov_b64 s[0:1], 0x800000
	v_lshl_add_u64 v[6:7], v[6:7], 0, s[0:1]
	v_mov_b32_e32 v5, v13
	v_mov_b32_e32 v3, v10
	s_cbranch_execz .LBB2_43
	s_branch .LBB2_44

.LBB2_46:
	v_mul_i32_i24_e32 v3, 0x320, v3
	v_lshlrev_b32_e32 v5, 4, v5
	v_add3_u32 v3, 0, v3, v5
	ds_read_b128 v[22:25], v3 offset:128
	v_cndmask_b32_e64 v3, 0, 1, s[4:5]
	v_lshl_add_u64 v[6:7], v[6:7], 1, s[10:11]
	v_cmp_ne_u32_e64 s[0:1], 1, v3
	s_andn2_b64 vcc, exec, s[4:5]
	s_waitcnt lgkmcnt(0)
	global_store_dwordx4 v[6:7], v[22:25], off sc1
	s_cbranch_vccnz .LBB2_49
	s_and_b64 vcc, exec, s[2:3]
	s_cbranch_vccnz .LBB2_50
	v_mov_b32_e32 v5, 0
	v_lshrrev_b32_e32 v3, 9, v15
	v_lshlrev_b64 v[6:7], 12, v[4:5]
	v_lshl_or_b32 v21, v3, 2, v13
	v_lshl_or_b32 v3, v3, 11, v6
	v_or_b32_e32 v6, v3, v1
	s_mov_b64 s[4:5], 0x800000
	v_lshl_add_u64 v[6:7], v[6:7], 0, s[4:5]
	v_mov_b32_e32 v3, v10
	s_cbranch_execz .LBB2_51
	s_branch .LBB2_52

.LBB2_54:
	v_lshlrev_b32_e32 v3, 1, v3
	v_mul_u32_u24_e32 v3, 0x190, v3
	v_lshlrev_b32_e32 v5, 4, v21
	v_add3_u32 v3, 0, v3, v5
	ds_read_b128 v[22:25], v3 offset:128
	v_lshl_add_u64 v[6:7], v[6:7], 1, s[10:11]
	s_and_b64 vcc, exec, s[0:1]
	s_waitcnt lgkmcnt(0)
	global_store_dwordx4 v[6:7], v[22:25], off sc1
	s_cbranch_vccnz .LBB2_57
	s_and_b64 vcc, exec, s[2:3]
	s_cbranch_vccnz .LBB2_58
	v_add_u32_e32 v6, 0x200, v4
	v_mov_b32_e32 v7, 0
	v_lshlrev_b64 v[6:7], 12, v[6:7]
	v_or_b32_e32 v6, v6, v1
	s_mov_b64 s[4:5], 0x800000
	v_lshl_add_u64 v[6:7], v[6:7], 0, s[4:5]
	v_mov_b32_e32 v3, v13
	v_mov_b32_e32 v5, v10
	s_cbranch_execz .LBB2_59
	s_branch .LBB2_60

.LBB2_62:
	v_mul_i32_i24_e32 v5, 0x320, v5
	v_lshlrev_b32_e32 v3, 4, v3
	v_add3_u32 v3, 0, v5, v3
	ds_read_b128 v[22:25], v3 offset:528
	v_lshl_add_u64 v[6:7], v[6:7], 1, s[10:11]
	s_and_b64 vcc, exec, s[0:1]
	s_waitcnt lgkmcnt(0)
	global_store_dwordx4 v[6:7], v[22:25], off sc1
	s_cbranch_vccnz .LBB2_65
	s_and_b64 vcc, exec, s[2:3]
	s_cbranch_vccnz .LBB2_66
	v_lshl_add_u32 v4, 1, 9, v4
	v_mov_b32_e32 v5, 0
	v_bfe_u32 v6, v16, 9, 1
	v_lshlrev_b64 v[4:5], 12, v[4:5]
	v_lshl_or_b32 v4, v6, 11, v4
	v_or_b32_e32 v4, v4, v1
	s_mov_b64 s[2:3], 0x800000
	v_lshl_or_b32 v3, v6, 2, v13
	v_lshl_add_u64 v[4:5], v[4:5], 0, s[2:3]
	v_mov_b32_e32 v6, v10
	s_cbranch_execz .LBB2_67
	s_branch .LBB2_68

.LBB2_70:
	v_lshl_or_b32 v2, v6, 1, 1
	v_mul_u32_u24_e32 v2, 0x190, v2
	v_lshlrev_b32_e32 v3, 4, v3
	v_add3_u32 v2, 0, v2, v3
	ds_read_b128 v[22:25], v2 offset:128
	s_add_i32 s7, s7, 2
	s_and_b32 s2, s7, 0x70
	s_cmp_lg_u32 s2, 16
	v_lshl_add_u64 v[2:3], v[4:5], 1, s[10:11]
	s_cselect_b64 s[2:3], -1, 0
	s_lshl_b32 s4, s7, 5
	s_waitcnt lgkmcnt(0)
	global_store_dwordx4 v[2:3], v[22:25], off sc1
	s_and_b32 s4, s4, 0x1e0
	v_cndmask_b32_e64 v3, 0, 1, s[2:3]
	v_add_u32_e32 v4, s4, v17
	v_add_u32_e32 v2, s4, v18
	s_lshl_b32 s7, s7, 11
	s_and_b64 vcc, exec, s[0:1]
	v_cmp_ne_u32_e64 s[2:3], 1, v3
	s_cbranch_vccnz .LBB2_73
	s_and_b64 vcc, exec, s[2:3]
	s_cbranch_vccnz .LBB2_74
	v_mov_b32_e32 v5, 0
	v_lshlrev_b64 v[6:7], 12, v[4:5]
	v_or_b32_e32 v6, v6, v1
	s_mov_b64 s[4:5], 0x800000
	v_lshl_add_u64 v[6:7], v[6:7], 0, s[4:5]
	v_mov_b32_e32 v5, v13
	v_mov_b32_e32 v3, v10
	s_cbranch_execz .LBB2_75
	s_branch .LBB2_76

.LBB2_78:
	v_mul_i32_i24_e32 v3, 0x320, v3
	v_lshlrev_b32_e32 v5, 4, v5
	v_add3_u32 v3, 0, v3, v5
	ds_read_b128 v[22:25], v3 offset:256
	v_lshl_add_u64 v[6:7], v[6:7], 1, s[10:11]
	s_and_b64 vcc, exec, s[0:1]
	s_waitcnt lgkmcnt(0)
	global_store_dwordx4 v[6:7], v[22:25], off sc1
	s_cbranch_vccnz .LBB2_81
	s_and_b64 vcc, exec, s[2:3]
	s_cbranch_vccnz .LBB2_82
	v_mov_b32_e32 v5, 0
	v_lshrrev_b32_e32 v3, 9, v15
	v_lshlrev_b64 v[6:7], 12, v[4:5]
	v_lshl_or_b32 v17, v3, 2, v13
	v_lshl_or_b32 v3, v3, 11, v6
	v_or_b32_e32 v6, v3, v1
	s_mov_b64 s[4:5], 0x800000
	v_lshl_add_u64 v[6:7], v[6:7], 0, s[4:5]
	v_mov_b32_e32 v3, v10
	s_cbranch_execz .LBB2_83
	s_branch .LBB2_84

.LBB2_86:
	v_lshlrev_b32_e32 v3, 1, v3
	v_mul_u32_u24_e32 v3, 0x190, v3
	v_lshlrev_b32_e32 v5, 4, v17
	v_add3_u32 v3, 0, v3, v5
	ds_read_b128 v[22:25], v3 offset:256
	v_lshl_add_u64 v[6:7], v[6:7], 1, s[10:11]
	s_and_b64 vcc, exec, s[0:1]
	s_waitcnt lgkmcnt(0)
	global_store_dwordx4 v[6:7], v[22:25], off sc1
	s_cbranch_vccnz .LBB2_89
	s_and_b64 vcc, exec, s[2:3]
	s_cbranch_vccnz .LBB2_90
	v_add_u32_e32 v6, 0x200, v4
	v_mov_b32_e32 v7, 0
	v_lshlrev_b64 v[6:7], 12, v[6:7]
	v_or_b32_e32 v6, v6, v1
	s_mov_b64 s[4:5], 0x800000
	v_lshl_add_u64 v[6:7], v[6:7], 0, s[4:5]
	v_mov_b32_e32 v3, v13
	v_mov_b32_e32 v5, v10
	s_cbranch_execz .LBB2_91
	s_branch .LBB2_92

.LBB2_94:
	v_mul_i32_i24_e32 v0, 0x320, v5
	v_lshlrev_b32_e32 v3, 4, v3
	v_add3_u32 v0, 0, v0, v3
	ds_read_b128 v[22:25], v0 offset:656
	v_lshl_add_u64 v[6:7], v[6:7], 1, s[10:11]
	s_and_b64 vcc, exec, s[0:1]
	s_waitcnt lgkmcnt(0)
	global_store_dwordx4 v[6:7], v[22:25], off sc1
	s_cbranch_vccnz .LBB2_97
	s_and_b64 vcc, exec, s[2:3]
	s_cbranch_vccnz .LBB2_98
	v_lshl_add_u32 v4, 1, 9, v4
	v_mov_b32_e32 v5, 0
	v_bfe_u32 v0, v16, 9, 1
	v_lshlrev_b64 v[4:5], 12, v[4:5]
	v_lshl_or_b32 v3, v0, 2, v13
	v_lshl_or_b32 v0, v0, 11, v4
	v_or_b32_e32 v4, v0, v1
	s_mov_b64 s[0:1], 0x800000
	v_lshl_add_u64 v[0:1], v[4:5], 0, s[0:1]
	s_cbranch_execz .LBB2_99
	s_branch .LBB2_100

.LBB2_102:
	v_lshl_or_b32 v2, v10, 1, 1
	v_mul_u32_u24_e32 v2, 0x190, v2
	v_lshlrev_b32_e32 v3, 4, v3
	v_add3_u32 v2, 0, v2, v3
	ds_read_b128 v[2:5], v2 offset:256
	v_lshl_add_u64 v[0:1], v[0:1], 1, s[10:11]
	s_waitcnt lgkmcnt(0)
	global_store_dwordx4 v[0:1], v[2:5], off sc1
	s_endpgm

.LBB3_45:
	v_cvt_pk_f16_f32 v50, v80, v81
	v_cvt_pk_f16_f32 v51, v82, v83
	v_cvt_pk_f16_f32 v52, v84, v85
	v_cvt_pk_f16_f32 v53, v86, v87
	ds_read_b64_tr_b16 v[54:55], v194 offset:32768
	ds_read_b64_tr_b16 v[56:57], v194 offset:33280
	v_add_f32_e32 v49, v80, v81
	v_add_f32_e32 v49, v49, v82
	v_add_f32_e32 v49, v49, v83
	ds_read_b64_tr_b16 v[58:59], v194 offset:33792
	ds_read_b64_tr_b16 v[60:61], v194 offset:34304
	s_waitcnt lgkmcnt(2)
	v_mfma_f32_32x32x16_f16 v[0:15], v[50:53], v[54:57], v[0:15]
	ds_read_b64_tr_b16 v[54:55], v194 offset:36864
	ds_read_b64_tr_b16 v[56:57], v194 offset:37376
	v_add_f32_e32 v49, v49, v84
	v_add_f32_e32 v49, v49, v85
	v_add_f32_e32 v49, v49, v86
	v_cvt_pk_f16_f32 v62, v88, v89
	v_cvt_pk_f16_f32 v63, v90, v91
	v_cvt_pk_f16_f32 v64, v92, v93
	v_cvt_pk_f16_f32 v65, v94, v95
	v_add_f32_e32 v49, v49, v87
	v_add_f32_e32 v49, v49, v88
	s_waitcnt lgkmcnt(0)
	v_mfma_f32_32x32x16_f16 v[16:31], v[50:53], v[54:57], v[16:31]
	v_add_f32_e32 v49, v49, v89
	v_add_f32_e32 v49, v49, v90
	ds_read_b64_tr_b16 v[66:67], v194 offset:37888
	ds_read_b64_tr_b16 v[68:69], v194 offset:38400
	v_add_f32_e32 v49, v49, v91
	v_add_f32_e32 v49, v49, v92
	v_add_f32_e32 v49, v49, v93
	v_add_f32_e32 v49, v49, v94
	v_mfma_f32_32x32x16_f16 v[0:15], v[62:65], v[58:61], v[0:15]
	v_cvt_pk_f16_f32 v50, v32, v33
	v_cvt_pk_f16_f32 v51, v34, v35
	v_cvt_pk_f16_f32 v52, v36, v37
	v_cvt_pk_f16_f32 v53, v38, v39
	ds_read_b64_tr_b16 v[54:55], v194 offset:34816
	ds_read_b64_tr_b16 v[56:57], v194 offset:35328
	v_add_f32_e32 v49, v49, v95
	v_add_f32_e32 v49, v49, v32
	s_waitcnt lgkmcnt(2)
	v_mfma_f32_32x32x16_f16 v[16:31], v[62:65], v[66:69], v[16:31]
	v_add_f32_e32 v49, v49, v33
	v_add_f32_e32 v32, v49, v34
	v_add_f32_e32 v49, v32, v35
	ds_read_b64_tr_b16 v[32:33], v194 offset:35840
	ds_read_b64_tr_b16 v[34:35], v194 offset:36352
	v_add_f32_e32 v36, v49, v36
	v_add_f32_e32 v36, v36, v37
	v_cvt_pk_f16_f32 v58, v40, v41
	s_waitcnt lgkmcnt(2)
	v_mfma_f32_32x32x16_f16 v[0:15], v[50:53], v[54:57], v[0:15]
	ds_read_b64_tr_b16 v[54:55], v194 offset:38912
	ds_read_b64_tr_b16 v[56:57], v194 offset:39424
	v_cvt_pk_f16_f32 v59, v42, v43
	v_cvt_pk_f16_f32 v60, v44, v45
	v_cvt_pk_f16_f32 v61, v46, v47
	ds_read_b64_tr_b16 v[62:63], v194 offset:39936
	ds_read_b64_tr_b16 v[64:65], v194 offset:40448
	v_add_f32_e32 v36, v36, v38
	v_add_f32_e32 v36, v36, v39
	s_waitcnt lgkmcnt(2)
	v_mfma_f32_32x32x16_f16 v[16:31], v[50:53], v[54:57], v[16:31]
	v_add_f32_e32 v36, v36, v40
	v_add_f32_e32 v36, v36, v41
	v_mfma_f32_32x32x16_f16 v[0:15], v[58:61], v[32:35], v[0:15]
	v_add_f32_e32 v32, v36, v42
	v_add_f32_e32 v32, v32, v43
	v_add_f32_e32 v32, v32, v44
	v_add_f32_e32 v32, v32, v45
	v_add_f32_e32 v32, v32, v46
	v_add_f32_e32 v32, v32, v47
	v_add_f32_e32 v32, v116, v32
	s_waitcnt lgkmcnt(0)
	v_mfma_f32_32x32x16_f16 v[16:31], v[58:61], v[62:65], v[16:31]
	v_mov_b32_e32 v33, v32
	s_nop 1
	v_permlane32_swap_b32_e32 v32, v33
	s_and_saveexec_b64 s[2:3], s[0:1]
	v_add_f32_e32 v32, v32, v33
	ds_write_b32 v196, v32 offset:49280
	s_or_b64 exec, exec, s[2:3]
	s_waitcnt lgkmcnt(0)
	ds_read_b128 v[32:35], v48 offset:49280
	ds_read_b128 v[36:39], v48 offset:49312
	s_lshl_b32 s2, s26, 12
	s_add_i32 s2, s2, 0
	v_lshlrev_b32_e32 v49, 1, v191
	s_waitcnt lgkmcnt(1)
	v_rcp_f32_e32 v40, v32
	v_rcp_f32_e32 v41, v33
	v_rcp_f32_e32 v42, v34
	v_rcp_f32_e32 v43, v35
	s_waitcnt lgkmcnt(0)
	v_rcp_f32_e32 v44, v36
	ds_read_b128 v[32:35], v48 offset:49344
	v_rcp_f32_e32 v45, v37
	v_rcp_f32_e32 v46, v38
	v_rcp_f32_e32 v47, v39
	ds_read_b128 v[36:39], v48 offset:49376
	v_lshlrev_b32_e32 v48, 9, v192
	v_add3_u32 v48, s2, v48, v49
	v_fma_mixlo_f16 v0, v0, v40, 0
	ds_write_b16 v48, v0 offset:51200
	v_fma_mixlo_f16 v0, v16, v40, 0
	ds_write_b16 v48, v0 offset:51264
	v_fma_mixlo_f16 v0, v1, v41, 0
	ds_write_b16 v48, v0 offset:51328
	v_fma_mixlo_f16 v0, v17, v41, 0
	ds_write_b16 v48, v0 offset:51392
	v_fma_mixlo_f16 v0, v2, v42, 0
	ds_write_b16 v48, v0 offset:51456
	v_fma_mixlo_f16 v0, v18, v42, 0
	ds_write_b16 v48, v0 offset:51520
	v_fma_mixlo_f16 v0, v3, v43, 0
	ds_write_b16 v48, v0 offset:51584
	v_fma_mixlo_f16 v0, v19, v43, 0
	ds_write_b16 v48, v0 offset:51648
	v_fma_mixlo_f16 v0, v4, v44, 0
	ds_write_b16 v48, v0 offset:52224
	v_fma_mixlo_f16 v0, v20, v44, 0
	ds_write_b16 v48, v0 offset:52288
	v_fma_mixlo_f16 v0, v5, v45, 0
	ds_write_b16 v48, v0 offset:52352
	v_fma_mixlo_f16 v0, v21, v45, 0
	s_waitcnt lgkmcnt(12)
	v_rcp_f32_e32 v32, v32
	ds_write_b16 v48, v0 offset:52416
	v_fma_mixlo_f16 v0, v6, v46, 0
	ds_write_b16 v48, v0 offset:52480
	v_fma_mixlo_f16 v0, v22, v46, 0
	v_rcp_f32_e32 v33, v33
	ds_write_b16 v48, v0 offset:52544
	v_fma_mixlo_f16 v0, v7, v47, 0
	ds_write_b16 v48, v0 offset:52608
	v_fma_mixlo_f16 v0, v23, v47, 0
	v_rcp_f32_e32 v34, v34
	ds_write_b16 v48, v0 offset:52672
	v_fma_mixlo_f16 v0, v8, v32, 0
	ds_write_b16 v48, v0 offset:53248
	v_fma_mixlo_f16 v0, v24, v32, 0
	v_rcp_f32_e32 v35, v35
	ds_write_b16 v48, v0 offset:53312
	v_fma_mixlo_f16 v0, v9, v33, 0
	ds_write_b16 v48, v0 offset:53376
	v_fma_mixlo_f16 v0, v25, v33, 0
	s_waitcnt lgkmcnt(14)
	v_rcp_f32_e32 v36, v36
	ds_write_b16 v48, v0 offset:53440
	v_fma_mixlo_f16 v0, v10, v34, 0
	ds_write_b16 v48, v0 offset:53504
	v_fma_mixlo_f16 v0, v26, v34, 0
	v_rcp_f32_e32 v37, v37
	ds_write_b16 v48, v0 offset:53568
	v_fma_mixlo_f16 v0, v11, v35, 0
	ds_write_b16 v48, v0 offset:53632
	v_fma_mixlo_f16 v0, v27, v35, 0
	v_rcp_f32_e32 v38, v38
	ds_write_b16 v48, v0 offset:53696
	v_fma_mixlo_f16 v0, v12, v36, 0
	ds_write_b16 v48, v0 offset:54272
	v_fma_mixlo_f16 v0, v28, v36, 0
	v_rcp_f32_e32 v39, v39
	ds_write_b16 v48, v0 offset:54336
	v_fma_mixlo_f16 v0, v13, v37, 0
	ds_write_b16 v48, v0 offset:54400
	v_fma_mixlo_f16 v0, v29, v37, 0
	ds_write_b16 v48, v0 offset:54464
	v_fma_mixlo_f16 v0, v14, v38, 0
	ds_write_b16 v48, v0 offset:54528
	v_fma_mixlo_f16 v0, v30, v38, 0
	s_add_i32 s0, s28, s27
	s_mov_b32 s1, 0
	ds_write_b16 v48, v0 offset:54592
	v_fma_mixlo_f16 v0, v15, v39, 0
	s_lshl_b64 s[0:1], s[0:1], 12
	ds_write_b16 v48, v0 offset:54656
	v_fma_mixlo_f16 v0, v31, v39, 0
	ds_write_b16 v48, v0 offset:54720
	s_add_u32 s0, s6, s0
	v_and_b32_e32 v0, 56, v193
	s_addc_u32 s1, s7, s1
	s_lshl_b32 s3, s8, 7
	v_lshlrev_b32_e32 v8, 1, v0
	s_and_b32 s4, s3, 0xfffff800
	v_lshrrev_b32_e32 v14, 3, v190
	v_add_u32_e32 v15, s2, v8
	s_add_u32 s0, s0, s4
	s_waitcnt lgkmcnt(0)
	v_lshl_add_u32 v0, v14, 7, v15
	v_or_b32_e32 v16, 8, v14
	s_addc_u32 s1, s1, 0
	s_and_b32 s3, s3, 0x780
	ds_read_b128 v[0:3], v0 offset:51200
	v_lshl_add_u32 v4, v16, 7, v15
	s_add_u32 s0, s0, s3
	ds_read_b128 v[4:7], v4 offset:51200
	s_addc_u32 s1, s1, 0
	v_mov_b32_e32 v9, 0
	v_lshl_add_u64 v[10:11], s[0:1], 0, v[8:9]
	v_lshlrev_b32_e32 v8, 12, v14
	v_lshl_add_u64 v[12:13], v[10:11], 0, v[8:9]
	v_lshlrev_b32_e32 v8, 12, v16
	s_waitcnt lgkmcnt(1)
	global_store_dwordx4 v[12:13], v[0:3], off sc1
	s_nop 1
	v_lshl_add_u64 v[0:1], v[10:11], 0, v[8:9]
	s_waitcnt lgkmcnt(0)
	global_store_dwordx4 v[0:1], v[4:7], off sc1
	s_nop 1
	v_or_b32_e32 v4, 16, v14
	v_lshl_add_u32 v0, v4, 7, v15
	v_or_b32_e32 v14, 24, v14
	ds_read_b128 v[0:3], v0 offset:51200
	v_lshlrev_b32_e32 v8, 12, v4
	v_lshl_add_u32 v4, v14, 7, v15
	ds_read_b128 v[4:7], v4 offset:51200
	v_lshl_add_u64 v[12:13], v[10:11], 0, v[8:9]
	v_lshlrev_b32_e32 v8, 12, v14
	s_waitcnt lgkmcnt(1)
	global_store_dwordx4 v[12:13], v[0:3], off sc1
	s_nop 1
	v_lshl_add_u64 v[0:1], v[10:11], 0, v[8:9]
	s_waitcnt lgkmcnt(0)
	global_store_dwordx4 v[0:1], v[4:7], off sc1
	s_endpgm
